# FF warms the code of the following kernel (FT) in its XCD L2 with plain loads after its last vmcnt wait
# speedup vs baseline: 1.0336x; 1.0041x over previous
.LBB3_39:
	s_waitcnt vmcnt(5)
	v_rcp_f32_e32 v2, v133
	s_waitcnt vmcnt(4)
	v_rcp_f32_e32 v3, v132
	s_waitcnt vmcnt(3)
	v_rcp_f32_e32 v4, v131
	v_cmp_lt_f32_e32 vcc, 0, v133
	s_waitcnt vmcnt(2)
	v_rcp_f32_e32 v5, v130
	s_waitcnt vmcnt(1)
	v_rcp_f32_e32 v6, v129
	v_cndmask_b32_e32 v2, 0, v2, vcc
	v_cmp_lt_f32_e32 vcc, 0, v132
	s_waitcnt vmcnt(0)
	v_rcp_f32_e32 v7, v128
	s_getpc_b64 s[36:37]
.Lff_pc:
	s_add_u32 s36, s36, (.Lff_code_end-.Lff_pc)&4294967295
	s_addc_u32 s37, s37, 0
	v_lshlrev_b32_e32 v183, 6, v0
	v_min_u32_e32 v183, 0x3300, v183
	global_load_dword v183, v183, s[36:37]
	s_mov_b32 s4, 0x42c80000
	v_cndmask_b32_e32 v3, 0, v3, vcc
	v_cmp_lt_f32_e32 vcc, 0, v131
	v_cmp_ngt_f32_e64 s[2:3], s4, v3
	s_mov_b64 s[6:7], 0
	v_cndmask_b32_e32 v4, 0, v4, vcc
	v_cmp_lt_f32_e32 vcc, 0, v130
	s_nop 1
	v_cndmask_b32_e32 v5, 0, v5, vcc
	v_cmp_lt_f32_e32 vcc, 0, v129
	s_nop 1
	v_cndmask_b32_e32 v6, 0, v6, vcc
	v_cmp_lt_f32_e32 vcc, 0, v128
	s_nop 1
	v_cndmask_b32_e32 v7, 0, v7, vcc
	v_cmp_ngt_f32_e32 vcc, s4, v2
	s_or_b64 s[2:3], vcc, s[2:3]
	v_cmp_ngt_f32_e32 vcc, s4, v4
	s_or_b64 s[2:3], s[2:3], vcc
	v_cmp_ngt_f32_e32 vcc, s4, v5
	s_or_b64 s[2:3], s[2:3], vcc
	v_cmp_ngt_f32_e32 vcc, s4, v6
	s_or_b64 s[2:3], s[2:3], vcc
	v_cmp_ngt_f32_e32 vcc, s4, v7
	s_or_b64 s[2:3], s[2:3], vcc
	v_cndmask_b32_e64 v8, 0, 1, s[2:3]
	v_cmp_ne_u32_e32 vcc, 0, v8
	s_cmp_eq_u64 vcc, 0
	s_cselect_b64 s[2:3], -1, 0
	v_cndmask_b32_e64 v8, 0, 1, s[2:3]
	s_nop 0
	v_readfirstlane_b32 s2, v8
	s_bitcmp0_b32 s2, 0
	s_cbranch_scc0 .LBB3_45
	s_cmp_lt_i32 s26, 4
	s_cbranch_scc1 .LBB3_46
	s_cmp_gt_i32 s26, 4
	s_cbranch_scc0 .LBB3_47
	s_mov_b64 s[4:5], -1
	v_mov_b32_e32 v8, 0
	s_cmp_gt_i32 s26, 5
	v_mov_b32_e32 v167, 0
	v_mov_b32_e32 v166, 0
	v_mov_b32_e32 v165, 0
	v_mov_b32_e32 v164, 0
	v_mov_b32_e32 v162, 0
	v_mov_b32_e32 v160, 0
	v_mov_b32_e32 v159, 0
	v_mov_b32_e32 v157, 0
	v_mov_b32_e32 v151, 0
	v_mov_b32_e32 v149, 0
	v_mov_b32_e32 v147, 0
	v_mov_b32_e32 v146, 0
	v_mov_b32_e32 v144, 0
	v_mov_b32_e32 v143, 0
	v_mov_b32_e32 v152, 0
	v_mov_b32_e32 v153, 0
	v_mov_b32_e32 v154, 0
	v_mov_b32_e32 v155, 0
	v_mov_b32_e32 v156, 0
	v_mov_b32_e32 v158, 0
	v_mov_b32_e32 v161, 0
	v_mov_b32_e32 v163, 0
	v_mov_b32_e32 v168, 0
	v_mov_b32_e32 v169, 0
	v_mov_b32_e32 v170, 0
	v_mov_b32_e32 v171, 0
	v_mov_b32_e32 v172, 0
	v_mov_b32_e32 v173, 0
	v_mov_b32_e32 v174, 0
	v_mov_b32_e32 v145, 0
	v_mov_b32_e32 v148, 0
	v_mov_b32_e32 v150, 0
	s_cbranch_scc0 .LBB3_50
	s_cmp_eq_u32 s26, 6
	s_cbranch_scc0 .LBB3_49
	v_mov_b32_e32 v145, 0
	v_mov_b32_e32 v148, 0
	v_mov_b32_e32 v150, 0
	v_mov_b32_e32 v143, 0
	v_mov_b32_e32 v144, 0
	v_mov_b32_e32 v146, 0
	v_mov_b32_e32 v147, 0
	v_mov_b32_e32 v149, 0
	v_mov_b32_e32 v151, 0
	v_mov_b32_e32 v152, 0
	v_mov_b32_e32 v153, 0
	v_mov_b32_e32 v154, 0
	v_mov_b32_e32 v155, 0
	v_mov_b32_e32 v156, 0
	v_mov_b32_e32 v158, 0
	v_mov_b32_e32 v161, 0
	v_mov_b32_e32 v163, 0
	v_mov_b32_e32 v157, 0
	v_mov_b32_e32 v159, 0
	v_mov_b32_e32 v160, 0
	v_mov_b32_e32 v162, 0
	v_mov_b32_e32 v164, 0
	v_mov_b32_e32 v165, 0
	v_mov_b32_e32 v166, 0
	v_mov_b32_e32 v167, 0
	v_mov_b32_e32 v168, 0
	v_mov_b32_e32 v169, 0
	v_mov_b32_e32 v170, 0
	v_mov_b32_e32 v171, 0
	v_mov_b32_e32 v172, 0
	v_mov_b32_e32 v173, 0
	v_mov_b32_e32 v174, 0
	v_fma_mix_f32 v148, v43, v7, v148 op_sel_hi:[1,0,0]
	v_fma_mix_f32 v150, v45, v7, v150 op_sel_hi:[1,0,0]
	v_fma_mix_f32 v143, v50, v7, v143 op_sel_hi:[1,0,0]
	v_fma_mix_f32 v144, v54, v7, v144 op_sel_hi:[1,0,0]
	v_fma_mix_f32 v146, v58, v7, v146 op_sel_hi:[1,0,0]
	v_fma_mix_f32 v147, v61, v7, v147 op_sel_hi:[1,0,0]
	v_fma_mix_f32 v149, v64, v7, v149 op_sel_hi:[1,0,0]
	v_fma_mix_f32 v151, v66, v7, v151 op_sel_hi:[1,0,0]
	v_fma_mix_f32 v152, v43, v7, v152 op_sel:[1,0,0] op_sel_hi:[1,0,0]
	v_fma_mix_f32 v153, v45, v7, v153 op_sel:[1,0,0] op_sel_hi:[1,0,0]
	v_fma_mix_f32 v154, v50, v7, v154 op_sel:[1,0,0] op_sel_hi:[1,0,0]
	v_fma_mix_f32 v155, v54, v7, v155 op_sel:[1,0,0] op_sel_hi:[1,0,0]
	v_fma_mix_f32 v156, v58, v7, v156 op_sel:[1,0,0] op_sel_hi:[1,0,0]
	v_fma_mix_f32 v158, v61, v7, v158 op_sel:[1,0,0] op_sel_hi:[1,0,0]
	v_fma_mix_f32 v161, v64, v7, v161 op_sel:[1,0,0] op_sel_hi:[1,0,0]
	v_fma_mix_f32 v163, v66, v7, v163 op_sel:[1,0,0] op_sel_hi:[1,0,0]
	v_fma_mix_f32 v157, v72, v7, v157 op_sel_hi:[1,0,0]
	v_fma_mix_f32 v159, v76, v7, v159 op_sel_hi:[1,0,0]
	v_fma_mix_f32 v160, v83, v7, v160 op_sel_hi:[1,0,0]
	v_fma_mix_f32 v162, v85, v7, v162 op_sel_hi:[1,0,0]
	v_fma_mix_f32 v164, v89, v7, v164 op_sel_hi:[1,0,0]
	v_fma_mix_f32 v165, v92, v7, v165 op_sel_hi:[1,0,0]
	v_fma_mix_f32 v166, v95, v7, v166 op_sel_hi:[1,0,0]
	v_fma_mix_f32 v167, v96, v7, v167 op_sel_hi:[1,0,0]
	v_fma_mix_f32 v168, v72, v7, v168 op_sel:[1,0,0] op_sel_hi:[1,0,0]
	v_fma_mix_f32 v169, v76, v7, v169 op_sel:[1,0,0] op_sel_hi:[1,0,0]
	v_fma_mix_f32 v170, v83, v7, v170 op_sel:[1,0,0] op_sel_hi:[1,0,0]
	v_fma_mix_f32 v171, v85, v7, v171 op_sel:[1,0,0] op_sel_hi:[1,0,0]
	v_fma_mix_f32 v172, v89, v7, v172 op_sel:[1,0,0] op_sel_hi:[1,0,0]
	v_fma_mix_f32 v173, v92, v7, v173 op_sel:[1,0,0] op_sel_hi:[1,0,0]
	v_fma_mix_f32 v174, v95, v7, v174 op_sel:[1,0,0] op_sel_hi:[1,0,0]
	v_fma_mix_f32 v145, v96, v7, v145 op_sel:[1,0,0] op_sel_hi:[1,0,0]
	s_branch .LBB3_50

.Lff_code_end:
	.section	.rodata,"a",@progbits
	.p2align	6, 0x0
	.amdhsa_kernel _Z6k_iterILb0ELb0EEvPKfS1_PKiPK15HIP_vector_typeIfLj4EES7_S1_S1_S3_S1_PfS8_S1_S3_PDF16_PS5_SA_PiSA_SB_
		.amdhsa_group_segment_fixed_size 5808
		.amdhsa_private_segment_fixed_size 0
		.amdhsa_kernarg_size 152
		.amdhsa_user_sgpr_count 2
		.amdhsa_user_sgpr_dispatch_ptr 0
		.amdhsa_user_sgpr_queue_ptr 0
		.amdhsa_user_sgpr_kernarg_segment_ptr 1
		.amdhsa_user_sgpr_dispatch_id 0
		.amdhsa_user_sgpr_kernarg_preload_length 0
		.amdhsa_user_sgpr_kernarg_preload_offset 0
		.amdhsa_user_sgpr_private_segment_size 0
		.amdhsa_uses_dynamic_stack 0
		.amdhsa_enable_private_segment 0
		.amdhsa_system_sgpr_workgroup_id_x 1
		.amdhsa_system_sgpr_workgroup_id_y 0
		.amdhsa_system_sgpr_workgroup_id_z 0
		.amdhsa_system_sgpr_workgroup_info 0
		.amdhsa_system_vgpr_workitem_id 0
		.amdhsa_next_free_vgpr 184
		.amdhsa_next_free_sgpr 40
		.amdhsa_accum_offset 184
		.amdhsa_reserve_vcc 1
		.amdhsa_float_round_mode_32 0
		.amdhsa_float_round_mode_16_64 0
		.amdhsa_float_denorm_mode_32 3
		.amdhsa_float_denorm_mode_16_64 3
		.amdhsa_dx10_clamp 1
		.amdhsa_ieee_mode 1
		.amdhsa_fp16_overflow 0
		.amdhsa_tg_split 0
		.amdhsa_exception_fp_ieee_invalid_op 0
		.amdhsa_exception_fp_denorm_src 0
		.amdhsa_exception_fp_ieee_div_zero 0
		.amdhsa_exception_fp_ieee_overflow 0
		.amdhsa_exception_fp_ieee_underflow 0
		.amdhsa_exception_fp_ieee_inexact 0
		.amdhsa_exception_int_div_zero 0
	.end_amdhsa_kernel

amdhsa.kernels:
  - .agpr_count:     0
    .args:
      - .actual_access:  read_only
        .address_space:  global
        .offset:         0
        .size:           8
        .value_kind:     global_buffer
      - .actual_access:  read_only
        .address_space:  global
        .offset:         8
        .size:           8
        .value_kind:     global_buffer
      - .actual_access:  read_only
        .address_space:  global
        .offset:         16
        .size:           8
        .value_kind:     global_buffer
      - .actual_access:  read_only
        .address_space:  global
        .offset:         24
        .size:           8
        .value_kind:     global_buffer
      - .actual_access:  write_only
        .address_space:  global
        .offset:         32
        .size:           8
        .value_kind:     global_buffer
      - .actual_access:  write_only
        .address_space:  global
        .offset:         40
        .size:           8
        .value_kind:     global_buffer
      - .actual_access:  write_only
        .address_space:  global
        .offset:         48
        .size:           8
        .value_kind:     global_buffer
      - .actual_access:  write_only
        .address_space:  global
        .offset:         56
        .size:           8
        .value_kind:     global_buffer
      - .actual_access:  write_only
        .address_space:  global
        .offset:         64
        .size:           8
        .value_kind:     global_buffer
      - .actual_access:  write_only
        .address_space:  global
        .offset:         72
        .size:           8
        .value_kind:     global_buffer
      - .actual_access:  write_only
        .address_space:  global
        .offset:         80
        .size:           8
        .value_kind:     global_buffer
      - .actual_access:  write_only
        .address_space:  global
        .offset:         88
        .size:           8
        .value_kind:     global_buffer
      - .actual_access:  write_only
        .address_space:  global
        .offset:         96
        .size:           8
        .value_kind:     global_buffer
      - .actual_access:  write_only
        .address_space:  global
        .offset:         104
        .size:           8
        .value_kind:     global_buffer
      - .actual_access:  write_only
        .address_space:  global
        .offset:         112
        .size:           8
        .value_kind:     global_buffer
    .group_segment_fixed_size: 67584
    .kernarg_segment_align: 8
    .kernarg_segment_size: 120
    .language:       OpenCL C
    .language_version:
      - 2
      - 0
    .max_flat_workgroup_size: 1024
    .name:           _Z6k_sortPKfS0_PKiS2_PiP15HIP_vector_typeIfLj4EEPfS7_S3_S7_S7_S3_S3_S6_S6_
    .private_segment_fixed_size: 0
    .sgpr_count:     35
    .sgpr_spill_count: 0
    .symbol:         _Z6k_sortPKfS0_PKiS2_PiP15HIP_vector_typeIfLj4EEPfS7_S3_S7_S7_S3_S3_S6_S6_.kd
    .uniform_work_group_size: 1
    .uses_dynamic_stack: false
    .vgpr_count:     40
    .vgpr_spill_count: 0
    .wavefront_size: 64
  - .agpr_count:     0
    .args:
      - .actual_access:  read_only
        .address_space:  global
        .offset:         0
        .size:           8
        .value_kind:     global_buffer
      - .actual_access:  read_only
        .address_space:  global
        .offset:         8
        .size:           8
        .value_kind:     global_buffer
      - .actual_access:  read_only
        .address_space:  global
        .offset:         16
        .size:           8
        .value_kind:     global_buffer
      - .actual_access:  read_only
        .address_space:  global
        .offset:         24
        .size:           8
        .value_kind:     global_buffer
      - .actual_access:  read_only
        .address_space:  global
        .offset:         32
        .size:           8
        .value_kind:     global_buffer
      - .actual_access:  read_only
        .address_space:  global
        .offset:         40
        .size:           8
        .value_kind:     global_buffer
      - .actual_access:  read_only
        .address_space:  global
        .offset:         48
        .size:           8
        .value_kind:     global_buffer
      - .actual_access:  write_only
        .address_space:  global
        .offset:         56
        .size:           8
        .value_kind:     global_buffer
    .group_segment_fixed_size: 145952
    .kernarg_segment_align: 8
    .kernarg_segment_size: 64
    .language:       OpenCL C
    .language_version:
      - 2
      - 0
    .max_flat_workgroup_size: 512
    .name:           _Z7k_finalPK15HIP_vector_typeIfLj4EES2_PKiS4_PKfS6_PKDF16_Pf
    .private_segment_fixed_size: 0
    .sgpr_count:     34
    .sgpr_spill_count: 0
    .symbol:         _Z7k_finalPK15HIP_vector_typeIfLj4EES2_PKiS4_PKfS6_PKDF16_Pf.kd
    .uniform_work_group_size: 1
    .uses_dynamic_stack: false
    .vgpr_count:     177
    .vgpr_spill_count: 0
    .wavefront_size: 64
  - .agpr_count:     0
    .args:
      - .actual_access:  read_only
        .address_space:  global
        .offset:         0
        .size:           8
        .value_kind:     global_buffer
      - .actual_access:  read_only
        .address_space:  global
        .offset:         8
        .size:           8
        .value_kind:     global_buffer
      - .actual_access:  read_only
        .address_space:  global
        .offset:         16
        .size:           8
        .value_kind:     global_buffer
      - .actual_access:  read_only
        .address_space:  global
        .offset:         24
        .size:           8
        .value_kind:     global_buffer
      - .actual_access:  read_only
        .address_space:  global
        .offset:         32
        .size:           8
        .value_kind:     global_buffer
      - .actual_access:  read_only
        .address_space:  global
        .offset:         40
        .size:           8
        .value_kind:     global_buffer
      - .actual_access:  read_only
        .address_space:  global
        .offset:         48
        .size:           8
        .value_kind:     global_buffer
      - .actual_access:  read_only
        .address_space:  global
        .offset:         56
        .size:           8
        .value_kind:     global_buffer
      - .actual_access:  read_only
        .address_space:  global
        .offset:         64
        .size:           8
        .value_kind:     global_buffer
      - .address_space:  global
        .offset:         72
        .size:           8
        .value_kind:     global_buffer
      - .actual_access:  read_only
        .address_space:  global
        .offset:         80
        .size:           8
        .value_kind:     global_buffer
      - .actual_access:  read_only
        .address_space:  global
        .offset:         88
        .size:           8
        .value_kind:     global_buffer
      - .actual_access:  read_only
        .address_space:  global
        .offset:         96
        .size:           8
        .value_kind:     global_buffer
      - .actual_access:  write_only
        .address_space:  global
        .offset:         104
        .size:           8
        .value_kind:     global_buffer
      - .address_space:  global
        .offset:         112
        .size:           8
        .value_kind:     global_buffer
      - .actual_access:  write_only
        .address_space:  global
        .offset:         120
        .size:           8
        .value_kind:     global_buffer
      - .actual_access:  write_only
        .address_space:  global
        .offset:         128
        .size:           8
        .value_kind:     global_buffer
      - .actual_access:  write_only
        .address_space:  global
        .offset:         136
        .size:           8
        .value_kind:     global_buffer
      - .actual_access:  write_only
        .address_space:  global
        .offset:         144
        .size:           8
        .value_kind:     global_buffer
    .group_segment_fixed_size: 30384
    .kernarg_segment_align: 8
    .kernarg_segment_size: 152
    .language:       OpenCL C
    .language_version:
      - 2
      - 0
    .max_flat_workgroup_size: 512
    .name:           _Z6k_iterILb1ELb0EEvPKfS1_PKiPK15HIP_vector_typeIfLj4EES7_S1_S1_S3_S1_PfS8_S1_S3_PDF16_PS5_SA_PiSA_SB_
    .private_segment_fixed_size: 0
    .sgpr_count:     102
    .sgpr_spill_count: 0
    .symbol:         _Z6k_iterILb1ELb0EEvPKfS1_PKiPK15HIP_vector_typeIfLj4EES7_S1_S1_S3_S1_PfS8_S1_S3_PDF16_PS5_SA_PiSA_SB_.kd
    .uniform_work_group_size: 1
    .uses_dynamic_stack: false
    .vgpr_count:     216
    .vgpr_spill_count: 0
    .wavefront_size: 64
  - .agpr_count:     0
    .args:
      - .actual_access:  read_only
        .address_space:  global
        .offset:         0
        .size:           8
        .value_kind:     global_buffer
      - .actual_access:  read_only
        .address_space:  global
        .offset:         8
        .size:           8
        .value_kind:     global_buffer
      - .actual_access:  read_only
        .address_space:  global
        .offset:         16
        .size:           8
        .value_kind:     global_buffer
      - .actual_access:  read_only
        .address_space:  global
        .offset:         24
        .size:           8
        .value_kind:     global_buffer
      - .actual_access:  read_only
        .address_space:  global
        .offset:         32
        .size:           8
        .value_kind:     global_buffer
      - .actual_access:  read_only
        .address_space:  global
        .offset:         40
        .size:           8
        .value_kind:     global_buffer
      - .actual_access:  read_only
        .address_space:  global
        .offset:         48
        .size:           8
        .value_kind:     global_buffer
      - .actual_access:  read_only
        .address_space:  global
        .offset:         56
        .size:           8
        .value_kind:     global_buffer
      - .actual_access:  read_only
        .address_space:  global
        .offset:         64
        .size:           8
        .value_kind:     global_buffer
      - .address_space:  global
        .offset:         72
        .size:           8
        .value_kind:     global_buffer
      - .actual_access:  read_only
        .address_space:  global
        .offset:         80
        .size:           8
        .value_kind:     global_buffer
      - .actual_access:  read_only
        .address_space:  global
        .offset:         88
        .size:           8
        .value_kind:     global_buffer
      - .actual_access:  read_only
        .address_space:  global
        .offset:         96
        .size:           8
        .value_kind:     global_buffer
      - .actual_access:  read_only
        .address_space:  global
        .offset:         104
        .size:           8
        .value_kind:     global_buffer
      - .actual_access:  read_only
        .address_space:  global
        .offset:         112
        .size:           8
        .value_kind:     global_buffer
      - .actual_access:  read_only
        .address_space:  global
        .offset:         120
        .size:           8
        .value_kind:     global_buffer
      - .actual_access:  read_only
        .address_space:  global
        .offset:         128
        .size:           8
        .value_kind:     global_buffer
      - .actual_access:  read_only
        .address_space:  global
        .offset:         136
        .size:           8
        .value_kind:     global_buffer
      - .actual_access:  read_only
        .address_space:  global
        .offset:         144
        .size:           8
        .value_kind:     global_buffer
    .group_segment_fixed_size: 5808
    .kernarg_segment_align: 8
    .kernarg_segment_size: 152
    .language:       OpenCL C
    .language_version:
      - 2
      - 0
    .max_flat_workgroup_size: 512
    .name:           _Z6k_iterILb0ELb0EEvPKfS1_PKiPK15HIP_vector_typeIfLj4EES7_S1_S1_S3_S1_PfS8_S1_S3_PDF16_PS5_SA_PiSA_SB_
    .private_segment_fixed_size: 0
    .sgpr_count:     46
    .sgpr_spill_count: 0
    .symbol:         _Z6k_iterILb0ELb0EEvPKfS1_PKiPK15HIP_vector_typeIfLj4EES7_S1_S1_S3_S1_PfS8_S1_S3_PDF16_PS5_SA_PiSA_SB_.kd
    .uniform_work_group_size: 1
    .uses_dynamic_stack: false
    .vgpr_count:     184
    .vgpr_spill_count: 0
    .wavefront_size: 64
  - .agpr_count:     0
    .args:
      - .actual_access:  read_only
        .address_space:  global
        .offset:         0
        .size:           8
        .value_kind:     global_buffer
      - .actual_access:  read_only
        .address_space:  global
        .offset:         8
        .size:           8
        .value_kind:     global_buffer
      - .actual_access:  read_only
        .address_space:  global
        .offset:         16
        .size:           8
        .value_kind:     global_buffer
      - .actual_access:  read_only
        .address_space:  global
        .offset:         24
        .size:           8
        .value_kind:     global_buffer
      - .actual_access:  read_only
        .address_space:  global
        .offset:         32
        .size:           8
        .value_kind:     global_buffer
      - .actual_access:  read_only
        .address_space:  global
        .offset:         40
        .size:           8
        .value_kind:     global_buffer
      - .actual_access:  read_only
        .address_space:  global
        .offset:         48
        .size:           8
        .value_kind:     global_buffer
      - .actual_access:  read_only
        .address_space:  global
        .offset:         56
        .size:           8
        .value_kind:     global_buffer
      - .actual_access:  read_only
        .address_space:  global
        .offset:         64
        .size:           8
        .value_kind:     global_buffer
      - .address_space:  global
        .offset:         72
        .size:           8
        .value_kind:     global_buffer
      - .actual_access:  write_only
        .address_space:  global
        .offset:         80
        .size:           8
        .value_kind:     global_buffer
      - .actual_access:  read_only
        .address_space:  global
        .offset:         88
        .size:           8
        .value_kind:     global_buffer
      - .actual_access:  read_only
        .address_space:  global
        .offset:         96
        .size:           8
        .value_kind:     global_buffer
      - .actual_access:  read_only
        .address_space:  global
        .offset:         104
        .size:           8
        .value_kind:     global_buffer
      - .actual_access:  read_only
        .address_space:  global
        .offset:         112
        .size:           8
        .value_kind:     global_buffer
      - .actual_access:  read_only
        .address_space:  global
        .offset:         120
        .size:           8
        .value_kind:     global_buffer
      - .actual_access:  read_only
        .address_space:  global
        .offset:         128
        .size:           8
        .value_kind:     global_buffer
      - .actual_access:  read_only
        .address_space:  global
        .offset:         136
        .size:           8
        .value_kind:     global_buffer
      - .actual_access:  read_only
        .address_space:  global
        .offset:         144
        .size:           8
        .value_kind:     global_buffer
    .group_segment_fixed_size: 5808
    .kernarg_segment_align: 8
    .kernarg_segment_size: 152
    .language:       OpenCL C
    .language_version:
      - 2
      - 0
    .max_flat_workgroup_size: 512
    .name:           _Z6k_iterILb0ELb1EEvPKfS1_PKiPK15HIP_vector_typeIfLj4EES7_S1_S1_S3_S1_PfS8_S1_S3_PDF16_PS5_SA_PiSA_SB_
    .private_segment_fixed_size: 0
    .sgpr_count:     42
    .sgpr_spill_count: 0
    .symbol:         _Z6k_iterILb0ELb1EEvPKfS1_PKiPK15HIP_vector_typeIfLj4EES7_S1_S1_S3_S1_PfS8_S1_S3_PDF16_PS5_SA_PiSA_SB_.kd
    .uniform_work_group_size: 1
    .uses_dynamic_stack: false
    .vgpr_count:     184
    .vgpr_spill_count: 0
    .wavefront_size: 64
